# memattn output: pairs of adjacent rows exchanged across lane pairs (DPP + v_perm) so 64 global_store_dword replace 128 global_store_short per wave item
# baseline (speedup 1.0000x reference)
.LBB0_533:
	ds_read_b128 v[0:3], v88
	ds_read_b128 v[90:93], v88 offset:32
	ds_read_b128 v[94:97], v88 offset:64
	ds_read_b128 v[98:101], v88 offset:96
	s_waitcnt lgkmcnt(3)
	v_mfma_f32_32x32x16_bf16 v[0:15], v[16:19], v[0:3], 0
	s_waitcnt lgkmcnt(2)
	v_mfma_f32_32x32x16_bf16 v[0:15], v[20:23], v[90:93], v[0:15]
	s_waitcnt lgkmcnt(1)
	v_mfma_f32_32x32x16_bf16 v[0:15], v[24:27], v[94:97], v[0:15]
	s_waitcnt lgkmcnt(0)
	v_mfma_f32_32x32x16_bf16 v[0:15], v[28:31], v[98:101], v[0:15]
	ds_read_b128 v[90:93], v88 offset:128
	ds_read_b128 v[94:97], v88 offset:160
	ds_read_b128 v[98:101], v88 offset:192
	ds_read_b128 v[102:105], v88 offset:224
	s_waitcnt lgkmcnt(3)
	v_mfma_f32_32x32x16_bf16 v[0:15], v[32:35], v[90:93], v[0:15]
	s_waitcnt lgkmcnt(2)
	v_mfma_f32_32x32x16_bf16 v[0:15], v[36:39], v[94:97], v[0:15]
	s_waitcnt lgkmcnt(1)
	v_mfma_f32_32x32x16_bf16 v[0:15], v[40:43], v[98:101], v[0:15]
	s_waitcnt lgkmcnt(0)
	v_mfma_f32_32x32x16_bf16 v[0:15], v[44:47], v[102:105], v[0:15]
	ds_read_b128 v[90:93], v88 offset:256
	ds_read_b128 v[94:97], v88 offset:288
	ds_read_b128 v[98:101], v88 offset:320
	ds_read_b128 v[102:105], v88 offset:352
	s_waitcnt lgkmcnt(3)
	v_mfma_f32_32x32x16_bf16 v[0:15], v[48:51], v[90:93], v[0:15]
	s_waitcnt lgkmcnt(2)
	v_mfma_f32_32x32x16_bf16 v[0:15], v[52:55], v[94:97], v[0:15]
	s_waitcnt lgkmcnt(1)
	v_mfma_f32_32x32x16_bf16 v[0:15], v[56:59], v[98:101], v[0:15]
	s_waitcnt lgkmcnt(0)
	v_mfma_f32_32x32x16_bf16 v[0:15], v[60:63], v[102:105], v[0:15]
	ds_read_b128 v[90:93], v88 offset:384
	ds_read_b128 v[94:97], v88 offset:416
	ds_read_b128 v[98:101], v88 offset:448
	ds_read_b128 v[102:105], v88 offset:480
	s_waitcnt lgkmcnt(3)
	v_mfma_f32_32x32x16_bf16 v[0:15], v[64:67], v[90:93], v[0:15]
	s_waitcnt lgkmcnt(2)
	v_mfma_f32_32x32x16_bf16 v[0:15], v[68:71], v[94:97], v[0:15]
	s_waitcnt lgkmcnt(1)
	v_mfma_f32_32x32x16_bf16 v[0:15], v[72:75], v[98:101], v[0:15]
	s_waitcnt lgkmcnt(0)
	v_mfma_f32_32x32x16_bf16 v[0:15], v[76:79], v[102:105], v[0:15]
	v_and_b32_e32 v106, 1, v175
	v_mov_b32_e32 v107, 0x5040100
	v_mov_b32_e32 v108, 0x3020706
	v_cmp_eq_u32_e32 vcc, 1, v106
	v_mul_u32_u24_e32 v100, 0x7fe, v106
	v_add_u32_e32 v88, 0x4200, v88
	v_mov_b32_e32 v98, s73
	v_mov_b32_e32 v99, 0
	v_mov_b32_e32 v101, 0
	v_cndmask_b32_e32 v107, v107, v108, vcc
	v_lshl_add_u64 v[98:99], v[98:99], 0, s[8:9]
	v_lshl_add_u64 v[98:99], v[98:99], 0, v[100:101]
	v_lshl_add_u64 v[90:91], v[80:81], 0, v[98:99]
	v_cvt_pk_bf16_f32 v110, v0, v1
	v_cvt_pk_bf16_f32 v111, v2, v3
	s_nop 1
	v_mov_b32_dpp v112, v110 quad_perm:[1,0,3,2] row_mask:0xf bank_mask:0xf
	v_mov_b32_dpp v113, v111 quad_perm:[1,0,3,2] row_mask:0xf bank_mask:0xf
	v_perm_b32 v110, v112, v110, v107
	v_perm_b32 v111, v113, v111, v107
	global_store_dword v[90:91], v110, off offset:-4096
	global_store_dword v[90:91], v111, off
	v_lshl_add_u64 v[92:93], v[84:85], 0, v[98:99]
	v_cvt_pk_bf16_f32 v114, v4, v5
	v_cvt_pk_bf16_f32 v115, v6, v7
	s_nop 1
	v_mov_b32_dpp v116, v114 quad_perm:[1,0,3,2] row_mask:0xf bank_mask:0xf
	v_mov_b32_dpp v117, v115 quad_perm:[1,0,3,2] row_mask:0xf bank_mask:0xf
	v_perm_b32 v114, v116, v114, v107
	v_perm_b32 v115, v117, v115, v107
	global_store_dword v[92:93], v114, off offset:-4096
	global_store_dword v[92:93], v115, off
	v_lshl_add_u64 v[94:95], v[86:87], 0, v[98:99]
	v_cvt_pk_bf16_f32 v118, v8, v9
	v_cvt_pk_bf16_f32 v119, v10, v11
	s_nop 1
	v_mov_b32_dpp v120, v118 quad_perm:[1,0,3,2] row_mask:0xf bank_mask:0xf
	v_mov_b32_dpp v121, v119 quad_perm:[1,0,3,2] row_mask:0xf bank_mask:0xf
	v_perm_b32 v118, v120, v118, v107
	v_perm_b32 v119, v121, v119, v107
	global_store_dword v[94:95], v118, off offset:-4096
	global_store_dword v[94:95], v119, off
	v_lshl_add_u64 v[96:97], v[82:83], 0, v[98:99]
	v_cvt_pk_bf16_f32 v122, v12, v13
	v_cvt_pk_bf16_f32 v123, v14, v15
	s_nop 1
	v_mov_b32_dpp v124, v122 quad_perm:[1,0,3,2] row_mask:0xf bank_mask:0xf
	v_mov_b32_dpp v125, v123 quad_perm:[1,0,3,2] row_mask:0xf bank_mask:0xf
	v_perm_b32 v122, v124, v122, v107
	v_perm_b32 v123, v125, v123, v107
	global_store_dword v[96:97], v122, off offset:-4096
	global_store_dword v[96:97], v123, off
	s_add_u32 s8, s8, 64
	s_addc_u32 s9, s9, 0
	s_cmpk_lg_i32 s8, 0x200
	s_cbranch_scc1 .LBB0_533
	s_add_i32 s16, s16, 1
	s_mov_b64 s[10:11], 0
	s_branch .LBB0_526
